# grid barrier: XCD leader no longer waits for its (non-returning) generation-word publish to complete before leaving the barrier
# baseline (speedup 1.0000x reference)
.LBB0_158:
	s_or_b64 exec, exec, s[6:7]
.LBB0_159:
	s_or_b64 exec, exec, s[0:1]
	s_add_u32 s0, s72, 0x278
	s_addc_u32 s1, s73, 0
	s_add_u32 s84, s54, 0x200
	s_addc_u32 s85, s55, 0
	s_add_u32 s60, s54, 0x1000
	s_addc_u32 s61, s55, 0
	s_add_u32 s62, s54, 0x1100
	s_addc_u32 s63, s55, 0
	s_add_u32 s64, s54, 0x1200
	s_addc_u32 s65, s55, 0
	s_add_u32 s66, s54, 0x1300
	v_writelane_b32 v255, s0, 0
	s_addc_u32 s67, s55, 0
	s_mov_b64 s[82:83], 0x1000
	v_writelane_b32 v255, s1, 1
	s_add_u32 s0, s54, 0x3400
	s_addc_u32 s1, s55, 0
	v_writelane_b32 v255, s0, 2
	v_mbcnt_lo_u32_b32 v2, -1, 0
	v_mbcnt_hi_u32_b32 v217, -1, v2
	v_writelane_b32 v255, s1, 3
	s_add_u32 s0, s54, 0x3500
	s_addc_u32 s1, s55, 0
	v_writelane_b32 v255, s0, 4
	v_and_b32_e32 v2, 64, v217
	v_add_u32_e32 v219, 64, v2
	v_writelane_b32 v255, s1, 5
	s_mov_b64 s[0:1], 0
	v_writelane_b32 v255, s0, 6
	v_mov_b32_e32 v2, 0x80
	s_mov_b32 s86, 0x8800
	v_writelane_b32 v255, s1, 7
	s_add_i32 s0, 0, 0x20000
	v_writelane_b32 v255, s0, 8
	s_add_i32 s0, 0, 0x20004
	v_writelane_b32 v255, s0, 9
	s_add_i32 s0, 0, 0x4400
	v_writelane_b32 v255, s0, 10
	s_add_i32 s0, 0, 0x11c00
	v_writelane_b32 v255, s0, 11
	s_mov_b32 s0, 0
	v_writelane_b32 v255, s0, 12
	v_mov_b32_e32 v227, 0
	s_mov_b32 s49, 0x8000
	v_writelane_b32 v255, s1, 13
	v_writelane_b32 v255, s72, 14
	s_movk_i32 s3, 0x7fff
	v_mov_b32_e32 v169, 0x358637bd
	v_writelane_b32 v255, s73, 15
	v_writelane_b32 v255, s74, 16
	v_writelane_b32 v255, s80, 17
	s_mov_b32 s58, 0x800000
	s_mov_b32 s88, 0x87ff
	v_writelane_b32 v255, s81, 18
	v_writelane_b32 v255, s60, 19
	s_movk_i32 s87, 0xff
	s_waitcnt lgkmcnt(0)
	v_mov_b32_e32 v1, 1
	v_writelane_b32 v255, s61, 20
	v_writelane_b32 v255, s62, 21
	s_mov_b64 s[96:97], 0x80
	s_movk_i32 s53, 0x1000
	v_writelane_b32 v255, s63, 22
	v_writelane_b32 v255, s64, 23
	s_mov_b32 s92, 0x3fb8aa3b
	s_movk_i32 s59, 0xe00
	v_writelane_b32 v255, s65, 24
	v_writelane_b32 v255, s66, 25
	s_mov_b32 s93, 0x41000000
	s_movk_i32 s78, 0x108
	v_xor_b32_e32 v254, 32, v217
	v_xor_b32_e32 v218, 16, v217
	v_xor_b32_e32 v216, 1, v217
	v_mov_b32_e32 v170, 0x3f317218
	v_mov_b32_e32 v168, 0x3a27c5ac
	v_lshl_or_b32 v228, v217, 2, v2
	s_mov_b64 s[76:77], 0x8000
	s_mov_b64 s[90:91], 0x4000
	s_mov_b32 s56, 0
	v_writelane_b32 v255, s67, 26
	s_barrier
	s_branch .LBB0_162

.LBB0_257:
	s_or_b64 exec, exec, s[6:7]
.LBB0_258:
	s_or_b64 exec, exec, s[0:1]
	s_abs_i32 s7, s79
	s_waitcnt lgkmcnt(0)
	v_cvt_f32_u32_e32 v2, s7
	s_sub_i32 s5, 0, s7
	s_mov_b64 s[0:1], s[72:73]
	s_mov_b32 s4, s2
	v_rcp_iflag_f32_e32 v2, v2
	s_barrier
	v_mul_f32_e32 v2, 0x4f7ffffe, v2
	v_cvt_u32_f32_e32 v2, v2
	s_nop 0
	v_readfirstlane_b32 s6, v2
	s_mul_i32 s5, s5, s6
	s_mul_hi_u32 s5, s6, s5
	s_add_i32 s5, s6, s5
	v_writelane_b32 v255, s5, 27
	s_mul_hi_u32 s5, s5, 0x770
	s_mul_i32 s5, s5, s7
	s_sub_i32 s5, 0x770, s5
	s_sub_i32 s6, s5, s7
	s_cmp_ge_u32 s5, s7
	s_cselect_b32 s5, s6, s5
	s_sub_i32 s6, s5, s7
	s_cmp_ge_u32 s5, s7
	s_cselect_b32 s5, s6, s5
	s_cmp_eq_u32 s5, 0
	v_writelane_b32 v255, s7, 28
	s_cselect_b64 s[6:7], -1, 0
	s_cmp_lt_i32 s4, s5
	s_cselect_b64 s[8:9], -1, 0
	s_or_b64 s[6:7], s[6:7], s[8:9]
	s_and_b64 vcc, exec, s[6:7]
	s_cbranch_vccnz .LBB0_261
	s_sub_i32 s4, s4, s5
	s_and_b32 s4, s4, 3
	s_mul_i32 s8, s4, 0x20d0
	s_memrealtime s[4:5]
	s_memrealtime s[6:7]
	s_addk_i32 s8, 0x20d0
	s_waitcnt lgkmcnt(0)
	s_and_b32 s5, s8, 0xfff0
	s_mul_i32 s5, s5, 0xcccd
	s_lshr_b32 s5, s5, 20
	s_sub_i32 s6, s6, s4
	s_cmp_le_u32 s5, s6
	s_cbranch_scc1 .LBB0_261

.LBB0_324:
	s_or_b64 exec, exec, s[6:7]
.LBB0_325:
	s_mov_b32 s50, 0x87ff
	s_or_b64 exec, exec, s[0:1]
	s_mov_b64 s[24:25], s[72:73]
	v_mov_b32_e32 v86, v0
	s_mov_b32 s0, s2
	s_waitcnt lgkmcnt(0)
	s_barrier
	s_mov_b32 s33, 0x8800
	v_ashrrev_i32_e32 v2, 6, v86
	v_lshl_add_u32 v110, s0, 3, v2
	v_readlane_b32 s0, v255, 12
	v_cmp_gt_i32_e32 vcc, s86, v110
	s_mul_hi_u32 s44, s0, 0x180
	s_mul_i32 s45, s0, 0x180
	v_readlane_b32 s1, v255, 13
	s_and_saveexec_b64 s[26:27], vcc
	s_mov_b32 s48, 0xffff0000
	s_cbranch_execz .LBB0_367
	s_load_dwordx4 s[8:11], s[24:25], 0x50
	s_load_dwordx2 s[0:1], s[24:25], 0x60
	s_load_dwordx4 s[4:7], s[24:25], 0x78
	v_readlane_b32 s14, v255, 12
	s_mul_i32 s13, s14, 0xc00
	s_mul_hi_u32 s12, s14, 0xc00
	s_waitcnt lgkmcnt(0)
	s_add_u32 s8, s8, s13
	s_addc_u32 s9, s9, s12
	s_lshl_b32 s12, s14, 8
	s_mov_b32 s13, s56
	s_lshl_b64 s[12:13], s[12:13], 2
	s_add_u32 s10, s10, s12
	v_and_b32_e32 v79, 63, v86
	s_addc_u32 s11, s11, s13
	v_lshlrev_b32_e32 v14, 4, v79
	s_add_u32 s4, s4, s45
	v_lshlrev_b32_e32 v78, 1, v79
	v_and_b32_e32 v46, 15, v86
	global_load_dwordx4 v[2:5], v14, s[8:9]
	global_load_dwordx4 v[6:9], v14, s[8:9] offset:1024
	global_load_dwordx4 v[10:13], v14, s[8:9] offset:2048
	s_nop 0
	global_load_dwordx4 v[14:17], v14, s[10:11]
	s_load_dwordx2 s[8:9], s[24:25], 0x90
	s_addc_u32 s5, s5, s44
	v_lshl_or_b32 v226, s14, 7, v78
	v_lshlrev_b32_e32 v18, 4, v46
	v_lshlrev_b32_e32 v112, 3, v46
	v_lshl_add_u64 v[22:23], v[226:227], 2, s[0:1]
	s_add_u32 s0, s6, s45
	global_load_dwordx4 v[18:21], v18, s[4:5]
	s_addc_u32 s1, s7, s44
	global_load_dwordx2 v[114:115], v[22:23], off
	global_load_dwordx2 v[116:117], v112, s[4:5] offset:256
	global_load_dwordx2 v[118:119], v112, s[0:1] offset:256
	s_load_dwordx2 s[4:5], s[24:25], 0xc0
	v_readlane_b32 s15, v255, 13
	s_lshl_b64 s[0:1], s[14:15], 12
	s_waitcnt lgkmcnt(0)
	s_add_u32 s0, s8, s0
	v_lshlrev_b32_e32 v54, 3, v79
	s_addc_u32 s1, s9, s1
	v_and_b32_e32 v171, 0xf8, v54
	v_lshlrev_b32_e32 v34, 5, v79
	s_add_u32 s4, s4, s12
	v_lshlrev_b32_e32 v42, 2, v171
	global_load_dwordx4 v[22:25], v34, s[0:1] offset:2064
	global_load_dwordx4 v[26:29], v34, s[0:1] offset:2048
	s_addc_u32 s5, s5, s13
	global_load_dwordx4 v[30:33], v34, s[0:1] offset:16
	s_nop 0
	global_load_dwordx4 v[34:37], v34, s[0:1]
	s_nop 0
	global_load_dwordx4 v[38:41], v42, s[4:5] offset:16
	s_nop 0
	global_load_dwordx4 v[42:45], v42, s[4:5]
	v_cmp_lt_i32_e32 vcc, s3, v110
	s_and_saveexec_b64 s[0:1], vcc
	s_xor_b64 s[0:1], exec, s[0:1]
	v_and_b32_e32 v58, 0xff, v110
	s_or_saveexec_b64 s[0:1], s[0:1]
	v_mov_b32_e32 v55, 0xff
	v_ashrrev_i32_e32 v111, 31, v110
	s_xor_b64 exec, exec, s[0:1]
	v_lshrrev_b32_e32 v47, 20, v111
	v_add_u32_e32 v47, v110, v47
	v_and_b32_e32 v47, 0xfffff000, v47
	v_sub_u32_e32 v58, v110, v47
	v_mov_b32_e32 v55, 0xfff
	s_or_b64 exec, exec, s[0:1]
	s_load_dwordx2 s[28:29], s[24:25], 0x138
	v_lshlrev_b32_e32 v48, 2, v79
	v_lshlrev_b32_e32 v81, 2, v46
	v_lshlrev_b32_e32 v87, 1, v46
	s_movk_i32 s0, 0x1c00
	s_waitcnt lgkmcnt(0)
	v_mov_b64_e32 v[46:47], s[28:29]
	v_lshrrev_b32_e32 v84, 4, v79
	v_mad_i64_i32 v[88:89], s[0:1], v110, s0, v[46:47]
	v_lshlrev_b32_e32 v122, 1, v48
	v_mov_b32_e32 v123, v227
	v_lshlrev_b32_e32 v46, 7, v84
	v_mov_b32_e32 v47, v227
	v_lshl_add_u64 v[90:91], v[88:89], 0, v[122:123]
	v_lshl_add_u64 v[46:47], v[88:89], 0, v[46:47]
	v_lshlrev_b32_e32 v120, 1, v81
	v_mov_b32_e32 v121, v227
	v_add_co_u32_e32 v56, vcc, s53, v90
	v_lshl_add_u64 v[46:47], v[46:47], 0, v[120:121]
	s_nop 0
	v_addc_co_u32_e32 v57, vcc, 0, v91, vcc
	global_load_dwordx2 v[196:197], v[46:47], off offset:1536
	global_load_dwordx2 v[142:143], v[56:57], off offset:576
	global_load_dwordx2 v[140:141], v[56:57], off offset:1088
	s_load_dwordx4 s[20:23], s[24:25], 0x218
	s_waitcnt vmcnt(8)
	v_mov_b32_e32 v85, v24
	s_waitcnt vmcnt(7)
	v_mov_b32_e32 v24, v28
	s_waitcnt vmcnt(6)
	v_mov_b32_e32 v28, v31
	s_waitcnt vmcnt(5)
	v_mov_b32_e32 v31, v35
	v_and_b32_e32 v35, 16, v78
	v_ashrrev_i32_e32 v59, 31, v58
	s_waitcnt vmcnt(4)
	v_mov_b32_e32 v100, v39
	s_waitcnt vmcnt(3)
	v_mov_b32_e32 v39, v43
	v_and_or_b32 v35, v87, 6, v35
	v_and_b32_e32 v43, 28, v48
	v_lshlrev_b64 v[46:47], 8, v[58:59]
	v_lshlrev_b64 v[60:61], 7, v[58:59]
	s_waitcnt lgkmcnt(0)
	v_lshl_add_u64 v[46:47], s[22:23], 0, v[46:47]
	v_lshlrev_b32_e32 v82, 2, v43
	v_mov_b32_e32 v83, v227
	v_lshl_add_u64 v[60:61], s[20:21], 0, v[60:61]
	v_lshlrev_b32_e32 v92, 2, v35
	v_mov_b32_e32 v93, v227
	v_lshl_add_u64 v[46:47], v[46:47], 0, v[82:83]
	v_lshl_add_u64 v[60:61], v[60:61], 0, v[92:93]
	v_cmp_lt_i32_e32 vcc, v58, v55
	v_mov_b32_e32 v35, 0x1c00
	global_load_dwordx4 v[50:53], v[46:47], off offset:128
	s_nop 0
	global_load_dwordx4 v[46:49], v[46:47], off
	s_nop 0
	global_load_dwordx2 v[160:161], v[60:61], off offset:32
	global_load_dwordx2 v[158:159], v[60:61], off
	global_load_dwordx2 v[130:131], v[56:57], off offset:2112
	global_load_dwordx2 v[128:129], v[56:57], off offset:1600
	v_cndmask_b32_e32 v56, 0, v35, vcc
	v_cmp_lt_i32_e32 vcc, 0, v58
	v_mov_b32_e32 v35, 0xffffe400
	v_mov_b32_e32 v57, v227
	v_cndmask_b32_e64 v59, 0, -1, vcc
	v_cndmask_b32_e32 v58, 0, v35, vcc
	v_lshl_add_u64 v[94:95], v[88:89], 0, v[56:57]
	v_lshlrev_b32_e32 v124, 1, v54
	v_mov_b32_e32 v125, v227
	v_lshl_add_u64 v[96:97], v[88:89], 0, v[58:59]
	v_lshlrev_b32_e32 v126, 1, v87
	v_mov_b32_e32 v127, v227
	v_lshl_add_u64 v[66:67], v[94:95], 0, v[124:125]
	v_lshl_add_u64 v[70:71], v[96:97], 0, v[124:125]
	v_lshl_add_u64 v[74:75], v[88:89], 0, v[124:125]
	v_lshl_add_u64 v[98:99], v[88:89], 0, v[126:127]
	v_lshlrev_b32_e32 v226, 6, v84
	global_load_dwordx4 v[54:57], v[66:67], off offset:3648
	global_load_dwordx4 v[58:61], v[70:71], off offset:3648
	global_load_dwordx4 v[62:65], v[74:75], off offset:3648
	s_nop 0
	global_load_dwordx4 v[66:69], v[66:67], off offset:2624
	s_nop 0
	global_load_dwordx4 v[70:73], v[70:71], off offset:2624
	s_nop 0
	global_load_dwordx4 v[74:77], v[74:75], off offset:2624
	v_readlane_b32 s0, v255, 12
	global_load_dword v230, v[98:99], off offset:2560
	v_lshlrev_b32_e32 v98, 1, v78
	v_mov_b32_e32 v99, v227
	v_lshl_add_u64 v[98:99], v[88:89], 0, v[98:99]
	v_lshl_add_u64 v[88:89], v[88:89], 0, v[226:227]
	v_lshl_add_u64 v[88:89], v[88:89], 0, v[126:127]
	global_load_dword v231, v[98:99], off offset:2304
	global_load_dword v213, v[88:89], off offset:2048
	v_lshl_add_u64 v[88:89], v[94:95], 0, v[122:123]
	global_load_dwordx2 v[210:211], v[88:89], off offset:1024
	global_load_dwordx2 v[200:201], v[88:89], off offset:512
	v_lshl_add_u64 v[88:89], v[96:97], 0, v[122:123]
	global_load_dwordx2 v[206:207], v[88:89], off offset:1024
	global_load_dwordx2 v[208:209], v[88:89], off offset:512
	global_load_dwordx2 v[202:203], v[90:91], off offset:1024
	global_load_dwordx2 v[204:205], v[90:91], off offset:512
	global_load_dwordx2 v[198:199], v[90:91], off
	v_readlane_b32 s1, v255, 13
	s_cmp_lg_u32 s0, 3
	s_load_dwordx2 s[0:1], s[24:25], 0x200
	s_load_dwordx4 s[36:39], s[24:25], 0x1f0
	v_and_b32_e32 v35, 4, v86
	v_lshlrev_b32_e32 v80, 5, v84
	s_cselect_b64 s[30:31], -1, 0
	s_waitcnt lgkmcnt(0)
	v_lshl_add_u64 v[138:139], s[0:1], 0, v[122:123]
	s_load_dwordx2 s[0:1], s[24:25], 0x1e0
	v_cmp_eq_u32_e64 s[4:5], 0, v35
	v_mov_b32_e32 v35, v36
	v_mov_b32_e32 v36, v31
	v_mov_b32_e32 v31, v32
	v_mov_b32_e32 v32, v28
	v_and_b32_e32 v28, 8, v86
	s_waitcnt lgkmcnt(0)
	v_lshl_add_u64 v[144:145], s[0:1], 0, v[122:123]
	v_mov_b32_e32 v146, v19
	v_mov_b32_e32 v147, v21
	v_mov_b32_e32 v19, v20
	v_mov_b32_e32 v20, v15
	v_mov_b32_e32 v21, v17
	v_mov_b32_e32 v150, v7
	v_mov_b32_e32 v151, v9
	v_mov_b32_e32 v15, v16
	v_mov_b32_e32 v7, v8
	v_lshlrev_b64 v[8:9], 11, v[110:111]
	s_ashr_i32 s95, s94, 31
	v_mul_hi_u32_u24_e32 v17, 0xc0, v84
	v_mul_u32_u24_e32 v16, 0xc0, v84
	s_movk_i32 s0, 0x300
	v_cmp_gt_u32_e64 s[6:7], 16, v79
	v_cmp_eq_u32_e64 s[8:9], 0, v79
	v_mov_b32_e32 v43, v44
	v_mov_b32_e32 v44, v39
	v_mov_b32_e32 v39, v40
	v_mov_b32_e32 v40, v100
	v_cmp_lt_u32_e64 s[10:11], 31, v79
	v_cmp_lt_u32_e64 s[12:13], 39, v79
	v_cmp_lt_u32_e64 s[14:15], 47, v79
	v_cmp_eq_u32_e64 s[16:17], 0, v28
	v_lshl_add_u64 v[132:133], s[20:21], 0, v[92:93]
	v_lshl_add_u64 v[134:135], s[36:37], 0, v[122:123]
	v_lshl_add_u64 v[136:137], s[38:39], 0, v[122:123]
	v_mov_b32_e32 v28, v27
	v_mov_b32_e32 v27, v24
	v_mov_b32_e32 v24, v23
	v_mov_b32_e32 v23, v85
	v_mov_b32_e32 v148, v11
	v_mov_b32_e32 v149, v13
	v_mov_b32_e32 v152, v3
	v_mov_b32_e32 v153, v5
	v_mov_b32_e32 v11, v12
	v_mov_b32_e32 v3, v4
	v_lshl_add_u64 v[4:5], s[22:23], 0, v[82:83]
	v_lshl_or_b32 v8, v79, 3, v8
	s_lshl_b64 s[34:35], s[94:95], 11
	v_or_b32_e32 v12, 0x80, v81
	v_mov_b32_e32 v13, v227
	v_mad_i64_i32 v[16:17], s[0:1], v110, s0, v[16:17]
	s_mul_hi_i32 s37, s94, 0x300
	s_mul_i32 s36, s94, 0x300
	v_mov_b32_e32 v113, v227
	s_mov_b64 s[38:39], 0
	v_lshlrev_b32_e32 v154, 1, v226
	v_lshlrev_b32_e32 v156, 1, v80
	v_lshlrev_b32_e32 v226, 1, v78
	s_mov_b64 s[40:41], 0
	v_mov_b32_e32 v212, v110
	s_branch .LBB0_332

.LBB0_418:
	s_or_b64 exec, exec, s[6:7]
.LBB0_419:
	s_or_b64 exec, exec, s[0:1]
	s_mov_b64 s[4:5], s[72:73]
	s_mov_b32 s0, s2
	v_mov_b32_e32 v7, v0
	s_waitcnt lgkmcnt(0)
	s_barrier
	s_cmpk_gt_i32 s0, 0x3b7
	v_readfirstlane_b32 s16, v7
	s_cbranch_scc1 .LBB0_439
	v_bfe_i32 v4, v7, 27, 1
	v_lshlrev_b32_e32 v2, 4, v7
	v_lshrrev_b32_e32 v4, 22, v4
	v_add_u32_e32 v4, v2, v4
	v_and_b32_e32 v4, 0xfffffc00, v4
	v_ashrrev_i32_e32 v3, 31, v7
	v_sub_u32_e32 v4, v2, v4
	v_lshrrev_b32_e32 v3, 26, v3
	v_lshrrev_b32_e32 v5, 4, v4
	v_add_u32_e32 v3, v7, v3
	v_bitop3_b32 v5, v5, v4, 32 bitop3:0x6c
	v_ashrrev_i32_e32 v4, 31, v4
	v_ashrrev_i32_e32 v3, 6, v3
	v_lshrrev_b32_e32 v4, 26, v4
	v_lshlrev_b32_e32 v6, 3, v3
	v_add_u32_e32 v4, v5, v4
	v_and_b32_e32 v6, -16, v6
	v_ashrrev_i32_e32 v4, 6, v4
	v_add_u32_e32 v46, v4, v6
	v_mul_i32_i24_e32 v6, 64, v4
	v_lshlrev_b32_e32 v3, 5, v3
	v_sub_u32_e32 v5, v5, v6
	v_and_b32_e32 v3, 32, v3
	v_ashrrev_i16_sdwa v5, v1, sext(v5) dst_sel:DWORD dst_unused:UNUSED_PAD src0_sel:DWORD src1_sel:BYTE_0
	v_add_u32_e32 v2, 0x2000, v2
	v_add_u32_sdwa v47, v3, sext(v5) dst_sel:DWORD dst_unused:UNUSED_PAD src0_sel:DWORD src1_sel:WORD_0
	v_ashrrev_i32_e32 v3, 31, v2
	v_lshrrev_b32_e32 v3, 22, v3
	v_add_u32_e32 v3, v2, v3
	v_ashrrev_i32_e32 v3, 10, v3
	v_mul_i32_i24_e32 v5, 0x400, v3
	v_sub_u32_e32 v2, v2, v5
	v_lshrrev_b32_e32 v5, 4, v2
	v_bitop3_b32 v2, v5, v2, 32 bitop3:0x6c
	v_ashrrev_i32_e32 v6, 31, v2
	v_lshrrev_b32_e32 v6, 26, v6
	s_load_dwordx4 s[8:11], s[4:5], 0x1d0
	s_load_dwordx2 s[12:13], s[4:5], 0x1b0
	v_lshlrev_b32_e32 v5, 3, v3
	v_add_u32_e32 v6, v2, v6
	v_and_b32_e32 v5, -16, v5
	v_ashrrev_i32_e32 v8, 6, v6
	v_readlane_b32 s4, v255, 12
	v_add_u32_e32 v48, v8, v5
	v_and_b32_e32 v5, 0xc0, v6
	s_mul_hi_u32 s1, s4, 0x150000
	s_mul_i32 s4, s4, 0x150000
	v_lshlrev_b32_e32 v3, 5, v3
	v_sub_u32_e32 v2, v2, v5
	s_waitcnt lgkmcnt(0)
	s_add_u32 s17, s8, s4
	v_and_b32_e32 v3, 32, v3
	v_ashrrev_i16_sdwa v2, v1, sext(v2) dst_sel:DWORD dst_unused:UNUSED_PAD src0_sel:DWORD src1_sel:BYTE_0
	s_addc_u32 s18, s9, s1
	v_add_u32_sdwa v49, v3, sext(v2) dst_sel:DWORD dst_unused:UNUSED_PAD src0_sel:DWORD src1_sel:WORD_0
	v_and_b32_e32 v2, 3, v8
	s_mov_b32 s1, 0x1ffffe0
	v_lshrrev_b32_e32 v3, 2, v48
	v_lshlrev_b32_e32 v5, 1, v48
	v_and_or_b32 v2, v48, s1, v2
	v_and_b32_e32 v3, 4, v3
	v_and_b32_e32 v5, 24, v5
	v_or3_b32 v2, v2, v3, v5
	s_movk_i32 s20, 0x180
	v_mul_lo_u32 v2, v2, s20
	v_add_lshl_u32 v34, v2, v49, 1
	v_and_b32_e32 v2, 3, v4
	v_and_or_b32 v2, v46, s1, v2
	s_ashr_i32 s1, s0, 31
	s_lshr_b32 s6, s1, 29
	v_readlane_b32 s5, v255, 13
	s_add_i32 s6, s0, s6
	s_ashr_i32 s5, s16, 6
	s_ashr_i32 s7, s6, 3
	s_and_b32 s6, s6, -8
	s_ashr_i32 s4, s16, 8
	s_lshl_b32 s19, s5, 10
	s_sub_i32 s6, s0, s6
	s_cmp_lt_i32 s6, 0
	s_movk_i32 s8, 0x78
	s_cselect_b32 s8, s8, 0x77
	s_mul_i32 s6, s8, s6
	s_add_i32 s6, s6, s7
	s_mul_hi_i32 s7, s6, 0x92492493
	s_add_i32 s7, s7, s6
	s_lshr_b32 s8, s7, 31
	s_ashr_i32 s7, s7, 5
	s_add_i32 s7, s7, s8
	s_lshl_b32 s8, s7, 3
	s_mul_i32 s7, s7, 56
	s_sub_i32 s7, s6, s7
	s_bfe_i32 s6, s7, 0x80000
	s_bfe_u32 s6, s6, 0x3000c
	s_add_i32 s9, s7, s6
	s_bfe_i32 s6, s9, 0x80000
	s_and_b32 s9, s9, 0xf8
	s_sub_i32 s9, s7, s9
	s_sext_i32_i8 s9, s9
	s_sext_i32_i16 s14, s6
	s_add_i32 s30, s8, s9
	v_lshrrev_b32_e32 v3, 2, v46
	v_lshlrev_b32_e32 v4, 1, v46
	s_lshr_b32 s6, s14, 3
	s_lshl_b32 s15, s30, 8
	v_and_b32_e32 v3, 4, v3
	v_and_b32_e32 v4, 24, v4
	s_cmp_gt_i32 s7, 15
	v_or3_b32 v2, v2, v3, v4
	s_cselect_b64 s[8:9], -1, 0
	v_mul_lo_u32 v2, v2, s20
	s_and_b64 s[8:9], s[8:9], exec
	v_add_lshl_u32 v36, v2, v47, 1
	s_cselect_b32 s8, 0x80, 0
	v_add_u32_e32 v2, s15, v46
	v_mul_lo_u32 v2, v2, s20
	v_add_u32_e32 v3, s8, v47
	v_add_lshl_u32 v4, v2, v3, 1
	v_add_u32_e32 v2, s15, v48
	s_bitset1_b32 s15, 7
	v_add_u32_e32 v6, s15, v46
	v_mul_lo_u32 v6, v6, s20
	s_ashr_i32 s7, s14, 3
	v_add_lshl_u32 v226, v6, v3, 1
	v_add_u32_e32 v3, s15, v48
	s_mul_hi_i32 s15, s7, 0x18000
	s_mul_i32 s14, s7, 0x18000
	s_mov_b32 s9, s56
	v_add_u32_e32 v5, s8, v49
	s_or_b64 s[8:9], s[14:15], s[8:9]
	s_lshl_b64 s[8:9], s[8:9], 1
	s_add_u32 s14, s17, s8
	v_mul_lo_u32 v2, v2, s20
	v_mul_lo_u32 v3, v3, s20
	s_addc_u32 s15, s18, s9
	s_add_i32 s20, s19, 0
	s_add_i32 m0, s20, 0x10000
	s_add_i32 s21, s20, 0x2000
	global_load_lds_dwordx4 v36, s[14:15]
	s_add_i32 m0, s20, 0x12000
	v_add_lshl_u32 v2, v5, v2, 1
	global_load_lds_dwordx4 v34, s[14:15]
	s_mov_b32 m0, s20
	s_add_u32 s8, s14, 0x18000
	global_load_lds_dwordx4 v4, s[12:13]
	s_mov_b32 m0, s21
	s_addc_u32 s9, s15, 0
	global_load_lds_dwordx4 v2, s[12:13]
	s_add_i32 m0, s20, 0x14000
	s_add_i32 s22, s20, 0x4000
	global_load_lds_dwordx4 v36, s[8:9]
	s_add_i32 m0, s20, 0x16000
	s_add_i32 s23, s20, 0x6000
	global_load_lds_dwordx4 v34, s[8:9]
	s_mov_b32 m0, s22
	v_add_lshl_u32 v6, v3, v5, 1
	global_load_lds_dwordx4 v226, s[12:13]
	s_mov_b32 m0, s23
	v_mov_b32_e32 v37, v227
	global_load_lds_dwordx4 v6, s[12:13]
	v_mov_b32_e32 v35, v227
	v_mov_b32_e32 v5, v227
	v_mov_b32_e32 v3, v227
	s_movk_i32 s43, 0x180
	v_lshl_add_u64 v[14:15], s[14:15], 0, v[36:37]
	v_lshl_add_u64 v[12:13], s[14:15], 0, v[34:35]
	v_lshl_add_u64 v[10:11], s[12:13], 0, v[4:5]
	s_cmp_lg_u32 s4, 1
	v_lshl_add_u64 v[8:9], s[12:13], 0, v[2:3]
	s_cbranch_scc1 .LBB0_422
	s_barrier

.LBB0_499:
	s_or_b64 exec, exec, s[6:7]
.LBB0_500:
	s_or_b64 exec, exec, s[0:1]
	s_mov_b64 s[0:1], s[72:73]
	v_mov_b32_e32 v31, v0
	s_waitcnt lgkmcnt(0)
	s_barrier
	s_mov_b32 s4, s2
	v_ashrrev_i32_e32 v2, 6, v31
	s_nop 0
	v_lshl_add_u32 v32, s4, 3, v2
	v_cmp_gt_i32_e32 vcc, s86, v32
	s_and_saveexec_b64 s[20:21], vcc
	s_cbranch_execz .LBB0_513
	s_load_dwordx2 s[4:5], s[0:1], 0x80
	s_load_dwordx2 s[6:7], s[0:1], 0x98
	s_load_dwordx2 s[8:9], s[0:1], 0xa8
	v_and_b32_e32 v58, 15, v31
	v_lshlrev_b32_e32 v2, 4, v58
	s_waitcnt lgkmcnt(0)
	s_add_u32 s4, s4, s45
	s_addc_u32 s5, s5, s44
	v_readlane_b32 s10, v255, 12
	global_load_dwordx4 v[2:5], v2, s[4:5]
	s_lshl_b32 s4, s10, 9
	s_mov_b32 s5, s56
	s_lshl_b64 s[4:5], s[4:5], 2
	s_add_u32 s6, s6, s4
	v_bfe_u32 v30, v31, 4, 2
	v_lshlrev_b32_e32 v74, 2, v58
	s_addc_u32 s7, s7, s5
	v_lshl_or_b32 v64, v30, 6, v74
	s_add_u32 s4, s8, s4
	v_lshlrev_b32_e32 v26, 2, v64
	s_addc_u32 s5, s9, s5
	global_load_dwordx4 v[6:9], v26, s[6:7]
	global_load_dwordx4 v[10:13], v26, s[6:7] offset:1024
	global_load_dwordx4 v[14:17], v26, s[4:5]
	global_load_dwordx4 v[18:21], v26, s[4:5] offset:1024
	s_load_dwordx4 s[4:7], s[0:1], 0xc8
	s_lshl_b32 s8, s10, 8
	s_mov_b32 s9, s56
	s_lshl_b64 s[8:9], s[8:9], 2
	v_and_b32_e32 v36, 63, v31
	s_waitcnt lgkmcnt(0)
	s_add_u32 s4, s4, s8
	s_addc_u32 s5, s5, s9
	global_load_dwordx4 v[22:25], v26, s[4:5]
	s_add_u32 s4, s6, s8
	s_addc_u32 s5, s7, s9
	s_load_dwordx2 s[6:7], s[0:1], 0x1d8
	global_load_dwordx4 v[26:29], v26, s[4:5]
	v_lshlrev_b32_e32 v226, 3, v36
	v_readlane_b32 s11, v255, 13
	v_ashrrev_i32_e32 v33, 31, v32
	s_waitcnt lgkmcnt(0)
	v_mov_b64_e32 v[34:35], s[6:7]
	v_mad_i64_i32 v[34:35], s[4:5], v32, s59, v[34:35]
	v_lshl_add_u64 v[34:35], v[34:35], 0, v[226:227]
	global_load_dwordx2 v[72:73], v[34:35], off
	global_load_dwordx2 v[54:55], v[34:35], off offset:512
	global_load_dwordx2 v[52:53], v[34:35], off offset:1024
	global_load_dwordx2 v[44:45], v[34:35], off offset:1536
	global_load_dwordx2 v[50:51], v[34:35], off offset:2048
	global_load_dwordx2 v[42:43], v[34:35], off offset:2560
	s_load_dwordx8 s[8:15], s[0:1], 0x180
	s_load_dwordx2 s[24:25], s[0:1], 0x168
	v_lshlrev_b64 v[70:71], 9, v[32:33]
	v_lshlrev_b32_e32 v31, 2, v31
	v_and_b32_e32 v40, 60, v31
	s_waitcnt lgkmcnt(0)
	v_lshl_add_u64 v[34:35], s[8:9], 0, v[70:71]
	v_lshl_add_u64 v[34:35], v[34:35], 0, v[226:227]
	global_load_dwordx2 v[48:49], v[34:35], off
	v_lshl_add_u64 v[34:35], s[24:25], 0, v[70:71]
	v_lshl_add_u64 v[34:35], v[34:35], 0, v[226:227]
	global_load_dwordx2 v[56:57], v[34:35], off
	s_load_dwordx2 s[22:23], s[0:1], 0x1c8
	s_load_dwordx4 s[16:19], s[0:1], 0x1b8
	v_mov_b32_e32 v41, v227
	v_cmp_lt_i32_e32 vcc, v216, v219
	v_lshlrev_b32_e32 v76, 1, v58
	v_cmp_eq_u32_e64 s[4:5], 0, v58
	s_waitcnt lgkmcnt(0)
	v_lshl_add_u64 v[34:35], s[16:17], 0, v[70:71]
	v_lshl_add_u64 v[34:35], v[34:35], 0, v[226:227]
	global_load_dwordx2 v[46:47], v[34:35], off
	v_lshlrev_b64 v[34:35], 6, v[32:33]
	v_lshl_add_u64 v[34:35], s[18:19], 0, v[34:35]
	v_lshl_add_u64 v[34:35], v[34:35], 0, v[40:41]
	global_load_dword v75, v[34:35], off
	v_lshl_add_u64 v[34:35], v[32:33], 2, s[22:23]
	global_load_dword v99, v[34:35], off
	v_xor_b32_e32 v34, 2, v217
	v_cndmask_b32_e32 v31, v217, v216, vcc
	v_cmp_lt_i32_e32 vcc, v34, v219
	v_lshl_add_u64 v[38:39], s[16:17], 0, v[226:227]
	v_lshl_add_u64 v[40:41], s[18:19], 0, v[40:41]
	v_cndmask_b32_e32 v34, v217, v34, vcc
	v_lshlrev_b32_e32 v96, 2, v34
	v_xor_b32_e32 v34, 4, v217
	v_cmp_lt_i32_e32 vcc, v34, v219
	s_load_dwordx4 s[16:19], s[0:1], 0x150
	v_lshlrev_b32_e32 v58, 3, v58
	v_cndmask_b32_e32 v34, v217, v34, vcc
	v_lshlrev_b32_e32 v97, 2, v34
	v_xor_b32_e32 v34, 8, v217
	v_cmp_lt_i32_e32 vcc, v34, v219
	v_mov_b32_e32 v59, v227
	v_lshlrev_b64 v[62:63], 4, v[32:33]
	v_cndmask_b32_e32 v34, v217, v34, vcc
	s_ashr_i32 s95, s94, 31
	v_lshlrev_b32_e32 v31, 2, v31
	v_lshlrev_b32_e32 v98, 2, v34
	v_lshl_add_u64 v[36:37], s[24:25], 0, v[226:227]
	s_waitcnt lgkmcnt(0)
	v_lshl_add_u64 v[58:59], s[18:19], 0, v[58:59]
	s_waitcnt vmcnt(17)
	v_mov_b32_e32 v60, v3
	v_mov_b32_e32 v61, v5
	v_mov_b32_e32 v3, v4
	v_lshl_add_u64 v[4:5], s[6:7], 0, v[226:227]
	v_lshl_or_b32 v62, v30, 2, v62
	s_lshl_b64 s[18:19], s[94:95], 4
	v_lshlrev_b32_e32 v64, 1, v64
	v_mov_b32_e32 v65, v227
	v_lshl_add_u64 v[66:67], s[10:11], 0, v[70:71]
	s_lshl_b64 s[10:11], s[94:95], 9
	s_mov_b32 s88, 0x87ff
	s_mov_b32 s86, 0x8800
	v_lshl_add_u64 v[68:69], s[12:13], 0, v[70:71]
	v_lshl_add_u64 v[70:71], s[14:15], 0, v[70:71]
	s_mov_b64 s[12:13], 0
	s_waitcnt vmcnt(12)
	v_mov_b32_e32 v34, v22
	v_mov_b32_e32 v35, v24
	v_mov_b32_e32 v24, v23
	v_lshl_add_u64 v[22:23], s[8:9], 0, v[226:227]
	v_lshlrev_b32_e32 v226, 1, v74
	v_lshlrev_b32_e32 v74, 1, v76
	s_branch .LBB0_503

.LBB0_564:
	s_or_b64 exec, exec, s[6:7]
.LBB0_565:
	s_or_b64 exec, exec, s[0:1]
	s_mov_b64 s[4:5], s[72:73]
	s_waitcnt lgkmcnt(0)
	v_mov_b32_e32 v2, v0
	s_mov_b32 s0, s2
	s_barrier
	s_nop 0
	v_lshl_add_u32 v22, s0, 9, v2
	s_mov_b32 s0, 0x40000
	v_cmp_gt_i32_e32 vcc, s0, v22
	s_and_saveexec_b64 s[0:1], vcc
	s_cbranch_execz .LBB0_570
	s_load_dwordx4 s[8:11], s[4:5], 0x208
	s_lshl_b32 s12, s79, 9
	s_mov_b64 s[6:7], 0

.LBB0_895:
	s_or_b64 exec, exec, s[6:7]
.LBB0_896:
	s_or_b64 exec, exec, s[0:1]
	s_mov_b64 s[10:11], s[72:73]
	v_mov_b32_e32 v10, v0
	s_and_b64 s[0:1], s[38:39], exec
	s_mov_b32 s18, s2
	s_waitcnt lgkmcnt(0)
	s_barrier
	s_cselect_b32 s24, s49, 0x8800
	v_ashrrev_i32_e32 v13, 6, v10
	s_lshl_b32 s20, s18, 3
	v_add_u32_e32 v32, s20, v13
	v_cmp_gt_i32_e32 vcc, s24, v32
	s_and_saveexec_b64 s[0:1], vcc
	s_cbranch_execz .LBB0_905
	s_load_dwordx2 s[6:7], s[10:11], 0x88
	v_readlane_b32 s4, v255, 12
	v_readlane_b32 s5, v255, 13
	s_lshl_b32 s4, s4, 8
	s_mov_b32 s5, s56
	s_lshl_b64 s[8:9], s[4:5], 2
	s_load_dwordx2 s[12:13], s[10:11], 0xd8
	s_load_dwordx2 s[4:5], s[10:11], 0x160
	s_load_dwordx2 s[14:15], s[10:11], 0x140
	s_waitcnt lgkmcnt(0)
	s_add_u32 s16, s6, s8
	s_addc_u32 s17, s7, s9
	v_and_b32_e32 v30, 63, v10
	s_add_u32 s8, s12, s8
	v_lshlrev_b32_e32 v6, 4, v30
	s_addc_u32 s9, s13, s9
	s_load_dwordx2 s[6:7], s[10:11], 0x1e8
	global_load_dwordx4 v[2:5], v6, s[16:17]
	s_nop 0
	global_load_dwordx4 v[6:9], v6, s[8:9]
	s_load_dwordx2 s[8:9], s[10:11], 0x170
	s_load_dwordx2 s[16:17], s[10:11], 0x1d8
	s_load_dwordx2 s[12:13], s[10:11], 0x1a8
	s_mul_i32 s26, s79, 24
	s_waitcnt vmcnt(5)
	v_add_u32_e32 v26, s26, v32
	v_lshrrev_b32_e32 v10, 2, v10
	v_cmp_gt_i32_e32 vcc, s24, v26
	v_and_b32_e32 v226, 12, v10
	s_waitcnt lgkmcnt(0)
	v_lshl_add_u64 v[10:11], s[12:13], 0, v[226:227]
	v_cndmask_b32_e32 v16, v32, v26, vcc
	v_ashrrev_i32_e32 v17, 31, v16
	s_add_u32 s10, s6, 0x1100000
	v_lshl_add_u64 v[14:15], v[16:17], 4, v[10:11]
	v_mov_b64_e32 v[18:19], s[16:17]
	v_lshlrev_b32_e32 v226, 3, v30
	v_lshlrev_b64 v[20:21], 9, v[16:17]
	s_addc_u32 s11, s7, 0
	global_load_dword v12, v[14:15], off
	v_mad_i64_i32 v[14:15], s[12:13], v16, s59, v[18:19]
	v_or_b32_e32 v20, v20, v226
	v_subrev_u32_e32 v26, s94, v26
	v_lshl_add_u64 v[14:15], v[14:15], 0, v[226:227]
	v_lshl_add_u64 v[16:17], s[8:9], 0, v[20:21]
	v_lshl_add_u64 v[22:23], s[10:11], 0, v[20:21]
	v_lshl_add_u64 v[24:25], s[6:7], 0, v[20:21]
	v_lshl_add_u64 v[20:21], s[4:5], 0, v[20:21]
	v_cmp_gt_i32_e32 vcc, s24, v26
	global_load_dwordx2 v[14:15], v[14:15], off offset:3072
	v_ashrrev_i32_e32 v33, 31, v32
	global_load_dwordx2 v[16:17], v[16:17], off
	s_nop 0
	global_load_dwordx2 v[36:37], v[22:23], off
	global_load_dwordx2 v[38:39], v[24:25], off
	global_load_dwordx2 v[34:35], v[20:21], off
	v_cndmask_b32_e32 v20, v32, v26, vcc
	v_ashrrev_i32_e32 v21, 31, v20
	v_lshl_add_u64 v[22:23], v[20:21], 4, v[10:11]
	global_load_dword v60, v[22:23], off
	v_mad_i64_i32 v[22:23], s[12:13], v20, s59, v[18:19]
	v_lshlrev_b64 v[20:21], 9, v[20:21]
	v_lshl_add_u64 v[22:23], v[22:23], 0, v[226:227]
	v_or_b32_e32 v20, v20, v226
	global_load_dwordx2 v[62:63], v[22:23], off offset:3072
	v_lshl_add_u64 v[22:23], s[8:9], 0, v[20:21]
	global_load_dwordx2 v[64:65], v[22:23], off
	v_lshl_add_u64 v[22:23], s[10:11], 0, v[20:21]
	v_lshl_add_u64 v[24:25], s[6:7], 0, v[20:21]
	v_lshl_add_u64 v[20:21], s[4:5], 0, v[20:21]
	global_load_dwordx2 v[78:79], v[22:23], off
	global_load_dwordx2 v[80:81], v[24:25], off
	global_load_dwordx2 v[76:77], v[20:21], off
	v_subrev_u32_e32 v20, s94, v26
	v_cmp_gt_i32_e32 vcc, s24, v20
	s_waitcnt vmcnt(15)
	v_lshlrev_b32_e32 v40, 2, v30
	v_lshl_add_u64 v[30:31], s[14:15], 0, v[226:227]
	v_cndmask_b32_e32 v20, v32, v20, vcc
	v_ashrrev_i32_e32 v21, 31, v20
	v_lshl_add_u64 v[22:23], v[20:21], 4, v[10:11]
	global_load_dword v82, v[22:23], off
	v_mad_i64_i32 v[22:23], s[12:13], v20, s59, v[18:19]
	v_lshlrev_b64 v[20:21], 9, v[20:21]
	v_lshl_add_u64 v[22:23], v[22:23], 0, v[226:227]
	v_or_b32_e32 v20, v20, v226
	global_load_dwordx2 v[84:85], v[22:23], off offset:3072
	v_lshl_add_u64 v[22:23], s[8:9], 0, v[20:21]
	v_mad_i64_i32 v[18:19], s[12:13], v32, s59, v[18:19]
	global_load_dwordx2 v[86:87], v[22:23], off
	v_lshl_add_u64 v[22:23], s[10:11], 0, v[20:21]
	v_lshl_add_u64 v[18:19], v[18:19], 0, v[226:227]
	v_lshl_add_u64 v[24:25], s[6:7], 0, v[20:21]
	global_load_dwordx2 v[90:91], v[22:23], off
	global_load_dwordx2 v[92:93], v[24:25], off
	v_lshl_add_u64 v[20:21], s[4:5], 0, v[20:21]
	global_load_dwordx2 v[22:23], v[18:19], off offset:3072
	v_lshlrev_b64 v[18:19], 9, v[32:33]
	global_load_dwordx2 v[88:89], v[20:21], off
	v_lshl_add_u64 v[20:21], v[32:33], 4, v[10:11]
	v_or_b32_e32 v18, v18, v226
	global_load_dword v105, v[20:21], off
	v_lshl_add_u64 v[20:21], s[8:9], 0, v[18:19]
	global_load_dwordx2 v[26:27], v[20:21], off
	v_lshl_add_u64 v[20:21], s[10:11], 0, v[18:19]
	v_lshl_add_u64 v[28:29], s[6:7], 0, v[18:19]
	v_lshl_add_u64 v[18:19], s[4:5], 0, v[18:19]
	global_load_dwordx2 v[24:25], v[20:21], off
	s_nop 0
	global_load_dwordx2 v[20:21], v[28:29], off
	v_cmp_lt_i32_e32 vcc, v254, v219
	global_load_dwordx2 v[18:19], v[18:19], off
	v_lshlrev_b64 v[32:33], 11, v[32:33]
	v_cndmask_b32_e32 v28, v217, v254, vcc
	v_cmp_lt_i32_e32 vcc, v218, v219
	v_lshlrev_b32_e32 v100, 2, v28
	s_lshl_b32 s12, s79, 5
	v_cndmask_b32_e32 v28, v217, v218, vcc
	v_lshlrev_b32_e32 v101, 2, v28
	v_xor_b32_e32 v28, 8, v217
	v_cmp_lt_i32_e32 vcc, v28, v219
	v_or_b32_e32 v32, v32, v226
	v_lshl_add_u64 v[32:33], s[14:15], 0, v[32:33]
	v_cndmask_b32_e32 v28, v217, v28, vcc
	v_lshlrev_b32_e32 v102, 2, v28
	v_xor_b32_e32 v28, 4, v217
	v_cmp_lt_i32_e32 vcc, v28, v219
	s_mov_b64 s[14:15], 0x200
	s_ashr_i32 s13, s12, 31
	v_cndmask_b32_e32 v28, v217, v28, vcc
	v_lshlrev_b32_e32 v103, 2, v28
	v_xor_b32_e32 v28, 2, v217
	v_cmp_lt_i32_e32 vcc, v28, v219
	v_lshl_add_u64 v[32:33], v[32:33], 0, s[14:15]
	s_lshl_b64 s[14:15], s[12:13], 11
	v_cndmask_b32_e32 v28, v217, v28, vcc
	v_cmp_lt_i32_e32 vcc, v216, v219
	v_lshlrev_b32_e32 v104, 2, v28
	s_mul_i32 s13, s79, 40
	v_cndmask_b32_e32 v28, v217, v216, vcc
	s_mul_i32 s21, s79, 48
	s_mul_i32 s22, s79, 56
	s_add_i32 s18, s18, s79
	s_lshl_b32 s25, s79, 4
	v_lshlrev_b32_e32 v106, 2, v28
	s_waitcnt vmcnt(25)
	v_mov_b32_e32 v28, v3
	v_mov_b32_e32 v29, v5
	v_mov_b32_e32 v3, v4
	s_waitcnt vmcnt(24)
	v_mov_b32_e32 v4, v7
	v_mov_b32_e32 v5, v9
	v_mov_b32_e32 v7, v8
	v_lshl_add_u64 v[8:9], s[16:17], 0, v[226:227]
	s_add_i32 s13, s13, s20
	s_add_i32 s21, s21, s20
	s_add_i32 s22, s22, s20
	s_lshl_b32 s23, s18, 3
	s_add_i32 s25, s25, s20
	s_add_i32 s26, s26, s20
	s_add_i32 s27, s12, s20
	s_mov_b64 s[16:17], 0
	v_lshlrev_b32_e32 v107, 1, v40
	s_branch .LBB0_899

.LBB0_977:
	s_or_b64 exec, exec, s[6:7]
.LBB0_978:
	s_or_b64 exec, exec, s[0:1]
	s_mov_b64 s[6:7], s[72:73]
	s_waitcnt lgkmcnt(0)
	s_barrier
	s_load_dwordx2 s[4:5], s[6:7], 0x120
	s_load_dwordx2 s[8:9], s[6:7], 0x140
	s_load_dwordx2 s[0:1], s[6:7], 0x260
	s_load_dwordx2 s[10:11], s[6:7], 0x178
	s_and_b64 s[6:7], s[38:39], exec
	s_movk_i32 s6, 0x80
	s_cselect_b32 s25, s6, 0x88
	s_lshl_b32 s12, s25, 2
	v_readlane_b32 s7, v255, 27
	s_mul_hi_u32 s7, s12, s7
	v_readlane_b32 s14, v255, 28
	s_mul_i32 s7, s7, s14
	s_sub_i32 s7, s12, s7
	s_sub_i32 s13, s7, s14
	s_cmp_ge_u32 s7, s14
	s_cselect_b32 s7, s13, s7
	s_sub_i32 s13, s7, s14
	s_cmp_ge_u32 s7, s14
	s_cselect_b32 s7, s13, s7
	s_mov_b32 s26, s2
	s_mov_b32 s6, s2
	s_cmp_eq_u32 s7, 0
	s_cselect_b64 s[14:15], -1, 0
	s_cmp_lt_i32 s6, s7
	s_cselect_b64 s[16:17], -1, 0
	s_or_b64 s[14:15], s[14:15], s[16:17]
	s_and_b64 vcc, exec, s[14:15]
	s_cbranch_vccnz .LBB0_981
	s_sub_i32 s6, s6, s7
	s_and_b32 s6, s6, 3
	s_mul_i32 s13, s6, 0x1068
	s_memrealtime s[6:7]
	s_memrealtime s[14:15]
	s_addk_i32 s13, 0x1068
	s_waitcnt lgkmcnt(0)
	s_and_b32 s7, s13, 0x7ff8
	s_mulk_i32 s7, 0x6667
	s_lshr_b32 s7, s7, 19
	s_sub_i32 s13, s14, s6
	s_cmp_le_u32 s7, s13
	s_cbranch_scc1 .LBB0_981

.LBB0_1046:
	s_or_b64 exec, exec, s[6:7]
.LBB0_1047:
	s_or_b64 exec, exec, s[0:1]
	s_mov_b64 s[12:13], s[72:73]
	v_mov_b32_e32 v18, v0
	s_waitcnt lgkmcnt(0)
	s_barrier
	s_nop 0
	s_mov_b64 s[14:15], exec
	s_mov_b64 s[94:95], 0x40000
	s_load_dwordx2 s[4:5], s[12:13], 0x178
	s_load_dwordx2 s[6:7], s[12:13], 0x130
	s_load_dwordx2 s[8:9], s[12:13], 0x228
	s_load_dwordx2 s[10:11], s[12:13], 0x120
	s_load_dwordx2 s[32:33], s[12:13], 0x38
	s_load_dwordx2 s[34:35], s[12:13], 0xf0
	s_load_dwordx2 s[0:1], s[12:13], 0xe8
	v_readlane_b32 s20, v255, 12
	v_readlane_b32 s36, v255, 6
	v_readlane_b32 s37, v255, 7
	v_and_b32_e32 v229, 63, v18
	v_lshlrev_b32_e32 v230, 3, v229
	v_lshlrev_b32_e32 v231, 4, v229
	v_bfe_u32 v232, v18, 2, 4
	v_lshlrev_b32_e32 v232, 2, v232
	v_and_b32_e32 v233, 8, v18
	v_cmp_eq_u32_e64 s[26:27], 0, v233
	v_and_b32_e32 v233, 4, v18
	v_cmp_eq_u32_e64 s[28:29], 0, v233
	v_and_b32_e32 v233, 3, v18
	v_cmp_eq_u32_e64 s[30:31], 0, v233
	v_mov_b32_e32 v234, 0x358637bd
	v_lshlrev_b32_e32 v220, 4, v18
	v_and_b32_e32 v221, 15, v18
	v_lshrrev_b32_e32 v222, 4, v18
	v_lshlrev_b32_e32 v221, 10, v221
	v_lshl_or_b32 v221, v222, 4, v221
	v_lshrrev_b32_e32 v222, 6, v18
	s_nop 0
	v_readfirstlane_b32 s18, v222
	s_lshl_b32 s19, s2, 3
	s_add_i32 s18, s18, s19
	s_add_i32 s19, s24, 0x7ff
	s_lshr_b32 s19, s19, 11
	s_mul_i32 s18, s18, s19
	s_add_i32 s19, s18, s19
	s_min_i32 s19, s19, s24
	s_mov_b32 s25, 0xffff0000
	s_mul_i32 s16, s20, 9
	s_mov_b32 s17, 0
	s_movk_i32 s22, 0x6000
	s_mul_i32 s21, s16, s22
	s_waitcnt lgkmcnt(0)
	s_add_u32 s0, s0, s36
	s_addc_u32 s1, s1, s37
	global_load_dwordx4 v[116:119], v220, s[0:1]
	s_add_u32 s0, s0, 0x2000
	s_addc_u32 s1, s1, 0
	global_load_dwordx4 v[120:123], v220, s[0:1]
	s_add_u32 s0, s0, 0x2000
	s_addc_u32 s1, s1, 0
	global_load_dwordx4 v[124:127], v220, s[0:1]
	s_add_u32 s0, s0, 0x2000
	s_addc_u32 s1, s1, 0
	global_load_dwordx4 v[128:131], v220, s[0:1]
	s_add_u32 s0, s0, 0x2000
	s_addc_u32 s1, s1, 0
	global_load_dwordx4 v[132:135], v220, s[0:1]
	s_add_u32 s0, s0, 0x2000
	s_addc_u32 s1, s1, 0
	global_load_dwordx4 v[136:139], v220, s[0:1]
	s_add_u32 s0, s0, 0x2000
	s_addc_u32 s1, s1, 0
	global_load_dwordx4 v[140:143], v220, s[0:1]
	s_add_u32 s0, s0, 0x2000
	s_addc_u32 s1, s1, 0
	global_load_dwordx4 v[144:147], v220, s[0:1]
	s_cmp_lt_i32 s18, s19
	s_cbranch_scc0 .Ln2_idle
	s_lshl_b32 s0, s20, 12
	s_lshl_b32 s1, s20, 6
	s_lshl_b32 s23, s18, 11
	s_lshl_b32 s36, s18, 6
	s_add_u32 s10, s10, s21
	s_addc_u32 s11, s11, 0
	s_add_u32 s32, s32, s0
	s_addc_u32 s33, s33, 0
	s_add_u32 s34, s34, s1
	s_addc_u32 s35, s35, 0
	s_add_u32 s4, s4, s23
	s_addc_u32 s5, s5, 0
	s_add_u32 s6, s6, s23
	s_addc_u32 s7, s7, 0
	s_add_u32 s8, s8, s36
	s_addc_u32 s9, s9, 0
	global_load_dwordx4 v[172:175], v231, s[32:33] offset:0
	global_load_dwordx4 v[176:179], v231, s[32:33] offset:1024
	global_load_dwordx4 v[180:183], v231, s[32:33] offset:2048
	global_load_dwordx4 v[184:187], v231, s[32:33] offset:3072
	global_load_dword v235, v232, s[34:35]
	s_add_i32 s23, s18, 1
	s_cmp_lt_i32 s23, s19
	s_cselect_b32 s21, 1, 0
	s_bitcmp0_b32 s18, 0
	s_cselect_b32 s21, s21, 0
	s_lshl_b32 s23, s21, 11
	s_lshl_b32 s36, s21, 6
	v_add_u32_e32 v236, s23, v230
	v_add_u32_e32 v238, s23, v230
	v_add_u32_e32 v237, s36, v232
	global_load_dwordx2 v[2:3], v230, s[4:5] offset:0
	global_load_dwordx2 v[4:5], v230, s[4:5] offset:512
	global_load_dwordx2 v[6:7], v230, s[4:5] offset:1024
	global_load_dwordx2 v[8:9], v230, s[4:5] offset:1536
	global_load_dwordx2 v[10:11], v236, s[4:5] offset:0
	global_load_dwordx2 v[12:13], v236, s[4:5] offset:512
	global_load_dwordx2 v[14:15], v236, s[4:5] offset:1024
	global_load_dwordx2 v[16:17], v236, s[4:5] offset:1536
	s_lshr_b32 s23, s18, 12
	s_cmp_lt_i32 s18, 0x8000
	s_cselect_b32 s20, s23, 8
	s_mul_i32 s0, s20, s22
	s_add_u32 s0, s10, s0
	s_addc_u32 s1, s11, 0
	s_add_u32 s0, s0, 0x3000
	s_addc_u32 s1, s1, 0
	global_load_dwordx4 v[68:71], v231, s[0:1] offset:0
	global_load_dwordx4 v[72:75], v231, s[0:1] offset:1024
	global_load_dwordx4 v[76:79], v231, s[0:1] offset:2048
	global_load_dwordx4 v[80:83], v231, s[0:1] offset:3072
	s_add_u32 s0, s0, 0x1000
	s_addc_u32 s1, s1, 0
	global_load_dwordx4 v[52:55], v231, s[0:1] offset:0
	global_load_dwordx4 v[56:59], v231, s[0:1] offset:1024
	global_load_dwordx4 v[60:63], v231, s[0:1] offset:2048
	global_load_dwordx4 v[64:67], v231, s[0:1] offset:3072
	s_waitcnt vmcnt(28)
	ds_write_b128 v221, v[116:119] offset:0
	s_waitcnt vmcnt(27)
	ds_write_b128 v221, v[120:123] offset:512
	s_waitcnt vmcnt(26)
	ds_write_b128 v221, v[124:127] offset:16384
	s_waitcnt vmcnt(25)
	ds_write_b128 v221, v[128:131] offset:16896
	s_waitcnt vmcnt(24)
	ds_write_b128 v221, v[132:135] offset:32768
	s_waitcnt vmcnt(23)
	ds_write_b128 v221, v[136:139] offset:33280
	s_waitcnt vmcnt(22)
	ds_write_b128 v221, v[140:143] offset:49152
	s_waitcnt vmcnt(21)
	ds_write_b128 v221, v[144:147] offset:49664
	s_waitcnt vmcnt(0) lgkmcnt(0)
	s_barrier
	v_add_f32_e32 v52, 1.0, v52
	v_add_f32_e32 v53, 1.0, v53
	v_add_f32_e32 v54, 1.0, v54
	v_add_f32_e32 v55, 1.0, v55
	v_add_f32_e32 v56, 1.0, v56
	v_add_f32_e32 v57, 1.0, v57
	v_add_f32_e32 v58, 1.0, v58
	v_add_f32_e32 v59, 1.0, v59
	v_add_f32_e32 v60, 1.0, v60
	v_add_f32_e32 v61, 1.0, v61
	v_add_f32_e32 v62, 1.0, v62
	v_add_f32_e32 v63, 1.0, v63
	v_add_f32_e32 v64, 1.0, v64
	v_add_f32_e32 v65, 1.0, v65
	v_add_f32_e32 v66, 1.0, v66
	v_add_f32_e32 v67, 1.0, v67
	v_mul_f32_e32 v52, v172, v52
	v_mul_f32_e32 v53, v173, v53
	v_mul_f32_e32 v54, v174, v54
	v_mul_f32_e32 v55, v175, v55
	v_mul_f32_e32 v56, v176, v56
	v_mul_f32_e32 v57, v177, v57
	v_mul_f32_e32 v58, v178, v58
	v_mul_f32_e32 v59, v179, v59
	v_mul_f32_e32 v60, v180, v60
	v_mul_f32_e32 v61, v181, v61
	v_mul_f32_e32 v62, v182, v62
	v_mul_f32_e32 v63, v183, v63
	v_mul_f32_e32 v64, v184, v64
	v_mul_f32_e32 v65, v185, v65
	v_mul_f32_e32 v66, v186, v66
	v_mul_f32_e32 v67, v187, v67
	s_branch .Ln2_loop

.LBB0_1108:
	s_or_b64 exec, exec, s[6:7]
.LBB0_1109:
	s_or_b64 exec, exec, s[0:1]
	s_and_b64 s[4:5], s[38:39], exec
	s_movk_i32 s4, 0x80
	s_mov_b64 s[0:1], s[72:73]
	v_mov_b32_e32 v6, v0
	s_cselect_b32 s52, s4, 0x100
	s_mov_b32 s57, s2
	s_waitcnt lgkmcnt(0)
	s_barrier
	s_cmp_ge_i32 s57, s52
	s_cbranch_scc1 .LBB0_1170
	v_and_b32_e32 v3, 63, v217
	v_cmp_ne_u32_e32 vcc, 63, v3
	s_load_dwordx4 s[60:63], s[0:1], 0x230
	s_load_dwordx2 s[50:51], s[0:1], 0x240
	v_addc_co_u32_e32 v4, vcc, 0, v217, vcc
	v_cmp_gt_u32_e32 vcc, 62, v3
	v_lshlrev_b32_e32 v14, 2, v4
	v_ashrrev_i32_e32 v12, 6, v6
	v_cndmask_b32_e64 v4, 0, 2, vcc
	v_cmp_gt_u32_e32 vcc, 60, v3
	v_add_lshl_u32 v15, v4, v217, 2
	s_movk_i32 s6, 0x100
	v_cndmask_b32_e64 v4, 0, 4, vcc
	v_cmp_gt_u32_e32 vcc, 56, v3
	v_add_lshl_u32 v16, v4, v217, 2
	v_lshlrev_b32_e32 v10, 2, v6
	v_cndmask_b32_e64 v4, 0, 8, vcc
	v_cmp_gt_u32_e32 vcc, 48, v3
	v_add_lshl_u32 v17, v4, v217, 2
	v_and_b32_e32 v4, 64, v217
	v_cndmask_b32_e64 v3, 0, 16, vcc
	v_add_lshl_u32 v18, v3, v217, 2
	v_add_u32_e32 v3, -1, v217
	v_cmp_lt_i32_e32 vcc, v3, v4
	v_and_b32_e32 v2, 63, v6
	v_and_b32_e32 v26, 0x7ffffffe, v12
	v_cndmask_b32_e32 v3, v3, v217, vcc
	v_lshlrev_b32_e32 v19, 2, v3
	v_add_u32_e32 v3, -2, v217
	v_cmp_lt_i32_e32 vcc, v3, v4
	s_add_i32 s33, 0, 0x4000
	v_cmp_eq_u32_e64 s[4:5], 0, v6
	v_cndmask_b32_e32 v3, v3, v217, vcc
	v_lshlrev_b32_e32 v20, 2, v3
	v_add_u32_e32 v3, -4, v217
	v_cmp_lt_i32_e32 vcc, v3, v4
	v_cmp_gt_i32_e64 s[6:7], s6, v6
	v_cmp_gt_i32_e64 s[8:9], 64, v6
	v_cndmask_b32_e32 v3, v3, v217, vcc
	v_lshlrev_b32_e32 v21, 2, v3
	v_add_u32_e32 v3, -8, v217
	v_cmp_lt_i32_e32 vcc, v3, v4
	v_lshl_add_u32 v11, v6, 4, 0
	v_cmp_eq_u32_e64 s[10:11], 63, v2
	v_cndmask_b32_e32 v3, v3, v217, vcc
	v_lshlrev_b32_e32 v22, 2, v3
	v_add_u32_e32 v3, -16, v217
	v_cmp_lt_i32_e32 vcc, v3, v4
	v_lshl_add_u32 v13, v12, 2, 0
	v_cmp_lt_i32_e64 s[12:13], 0, v12
	v_cndmask_b32_e32 v3, v3, v217, vcc
	v_lshlrev_b32_e32 v23, 2, v3
	v_subrev_u32_e32 v3, 32, v217
	v_cmp_lt_i32_e32 vcc, v3, v4
	v_cmp_eq_u32_e64 s[14:15], 63, v6
	v_cmp_gt_i32_e64 s[16:17], 62, v6
	v_cndmask_b32_e32 v3, v3, v217, vcc
	v_cmp_gt_i32_e64 s[18:19], 60, v6
	v_cmp_gt_i32_e64 s[20:21], 56, v6
	v_cmp_gt_i32_e64 s[22:23], 48, v6
	v_cmp_gt_i32_e64 s[24:25], 32, v6
	v_cmp_eq_u32_e64 s[26:27], 0, v2
	v_cmp_gt_u32_e64 s[28:29], 2, v2
	v_cmp_gt_u32_e64 s[30:31], 4, v2
	v_cmp_gt_u32_e64 s[34:35], 8, v2
	v_cmp_gt_u32_e64 s[36:37], 16, v2
	v_lshlrev_b32_e32 v24, 2, v3
	v_cmp_gt_u32_e64 s[38:39], 32, v2
	v_not_b32_e32 v25, v6
	v_add_u32_e32 v7, 0x200, v6
	v_cmp_ne_u32_e64 s[40:41], 1, v12
	v_cmp_ne_u32_e64 s[42:43], v12, v26
	v_add_u32_e32 v27, 0, v10
	v_add_u32_e32 v28, s33, v10
	v_add_u32_e32 v29, 0xfffffe00, v6
	s_branch .LBB0_1112

.LBB0_1221:
	s_or_b64 exec, exec, s[6:7]
.LBB0_1222:
	s_or_b64 exec, exec, s[0:1]
	s_mov_b64 s[0:1], s[72:73]
	s_waitcnt lgkmcnt(0)
	s_barrier
	s_load_dwordx2 s[10:11], s[0:1], 0x130
	s_load_dwordx2 s[12:13], s[0:1], 0x268
	s_load_dwordx2 s[14:15], s[0:1], 0x230
	s_load_dwordx2 s[16:17], s[0:1], 0x248
	s_and_b64 s[0:1], s[38:39], exec
	s_movk_i32 s0, 0x110
	s_cselect_b32 s28, 0x100, s0
	s_lshl_b32 s18, s28, 3
	v_readlane_b32 s1, v255, 27
	s_mul_hi_u32 s1, s18, s1
	v_readlane_b32 s5, v255, 28
	s_mul_i32 s1, s1, s5
	s_sub_i32 s1, s18, s1
	s_sub_i32 s4, s1, s5
	s_cmp_ge_u32 s1, s5
	s_cselect_b32 s1, s4, s1
	s_sub_i32 s4, s1, s5
	s_cmp_ge_u32 s1, s5
	s_cselect_b32 s1, s4, s1
	s_mov_b32 s26, s2
	s_mov_b32 s0, s2
	s_cmp_eq_u32 s1, 0
	s_cselect_b64 s[4:5], -1, 0
	s_cmp_lt_i32 s0, s1
	s_cselect_b64 s[6:7], -1, 0
	s_or_b64 s[4:5], s[4:5], s[6:7]
	s_and_b64 vcc, exec, s[4:5]
	s_cbranch_vccnz .LBB0_1225
	s_sub_i32 s0, s0, s1
	s_and_b32 s0, s0, 3
	s_mul_i32 s6, s0, 0x20d0
	s_memrealtime s[0:1]
	s_memrealtime s[4:5]
	s_addk_i32 s6, 0x20d0
	s_waitcnt lgkmcnt(0)
	s_and_b32 s1, s6, 0xfff0
	s_mul_i32 s1, s1, 0xcccd
	s_lshr_b32 s1, s1, 20
	s_sub_i32 s4, s4, s0
	s_cmp_le_u32 s1, s4
	s_cbranch_scc1 .LBB0_1225

.LBB0_1306:
	s_or_b64 exec, exec, s[6:7]
.LBB0_1307:
	s_or_b64 exec, exec, s[0:1]
	s_mov_b64 s[0:1], s[72:73]
	s_waitcnt lgkmcnt(0)
	s_barrier
	s_load_dwordx2 s[12:13], s[0:1], 0x238
	s_load_dwordx4 s[8:11], s[0:1], 0x248
	s_load_dwordx2 s[14:15], s[0:1], 0x270
	s_lshl_b32 s16, s28, 2
	v_readlane_b32 s1, v255, 27
	s_mul_hi_u32 s1, s16, s1
	v_readlane_b32 s5, v255, 28
	s_mul_i32 s1, s1, s5
	s_sub_i32 s1, s16, s1
	s_sub_i32 s4, s1, s5
	s_cmp_ge_u32 s1, s5
	s_cselect_b32 s1, s4, s1
	s_sub_i32 s4, s1, s5
	s_cmp_ge_u32 s1, s5
	s_cselect_b32 s1, s4, s1
	s_mov_b32 s29, s2
	s_mov_b32 s0, s2
	s_cmp_eq_u32 s1, 0
	s_cselect_b64 s[4:5], -1, 0
	s_cmp_lt_i32 s0, s1
	s_cselect_b64 s[6:7], -1, 0
	s_or_b64 s[4:5], s[4:5], s[6:7]
	s_and_b64 vcc, exec, s[4:5]
	s_cbranch_vccnz .LBB0_1310
	s_sub_i32 s0, s0, s1
	s_and_b32 s0, s0, 3
	s_mul_i32 s6, s0, 0x20d0
	s_memrealtime s[0:1]
	s_memrealtime s[4:5]
	s_addk_i32 s6, 0x20d0
	s_waitcnt lgkmcnt(0)
	s_and_b32 s1, s6, 0xfff0
	s_mul_i32 s1, s1, 0xcccd
	s_lshr_b32 s1, s1, 20
	s_sub_i32 s4, s4, s0
	s_cmp_le_u32 s1, s4
	s_cbranch_scc1 .LBB0_1310
